# diff-attention loop: waves 4-7 sleep 384 clocks after each step barrier so the two waves of a SIMD run their MFMA and VALU sections out of phase
# baseline (speedup 1.0000x reference)
.LBB0_1354:
	v_readlane_b32 s98, v255, 63
	s_bitcmp1_b32 s98, 0
	s_cbranch_scc0 .Ldsy_0
	s_sleep 6

.LBB0_1360:
	v_lshl_add_u64 v[146:147], s[76:77], 0, v[194:195]
	v_add_co_u32_e32 v150, vcc, 0xc4000, v146
	v_lshl_add_u64 v[182:183], s[72:73], 0, v[194:195]
	s_nop 0
	v_addc_co_u32_e32 v151, vcc, 0, v147, vcc
	v_add_co_u32_e32 v154, vcc, 0x126000, v146
	s_nop 1
	v_addc_co_u32_e32 v155, vcc, 0, v147, vcc
	v_add_co_u32_e32 v184, vcc, 0xc4000, v182
	global_load_dwordx4 v[146:149], v[150:151], off
	s_nop 0
	global_load_dwordx4 v[150:153], v[150:151], off offset:256
	s_nop 0
	global_load_dwordx4 v[158:161], v[154:155], off
	s_nop 0
	global_load_dwordx4 v[154:157], v[154:155], off offset:256
	v_addc_co_u32_e32 v185, vcc, 0, v183, vcc
	v_add_co_u32_e32 v186, vcc, 0x126000, v182
	s_nop 1
	v_addc_co_u32_e32 v187, vcc, 0, v183, vcc
	global_load_dwordx4 v[182:185], v[184:185], off
	s_nop 0
	global_load_dwordx4 v[186:189], v[186:187], off
	s_setprio 1
	ds_read_b64_tr_b16 v[238:239], v213 offset:0
	ds_read_b64_tr_b16 v[240:241], v213 offset:0x1000
	ds_read_b64_tr_b16 v[244:245], v213 offset:0x2000
	ds_read_b64_tr_b16 v[246:247], v213 offset:0x3000
	ds_read_b64_tr_b16 v[250:251], v213 offset:0x4000
	ds_read_b64_tr_b16 v[252:253], v213 offset:0x5000
	ds_read_b64_tr_b16 v[206:207], v213 offset:0x6000
	ds_read_b64_tr_b16 v[208:209], v213 offset:0x7000
	s_waitcnt lgkmcnt(0)
	s_nop 0
	v_mfma_f32_32x32x16_bf16 v[114:129], v[130:133], v[238:241], v[114:129]
	v_mfma_f32_32x32x16_bf16 v[114:129], v[134:137], v[244:247], v[114:129]
	v_mfma_f32_32x32x16_bf16 v[114:129], v[138:141], v[250:253], v[114:129]
	v_mfma_f32_32x32x16_bf16 v[114:129], v[142:145], v[206:209], v[114:129]
	ds_read_b64_tr_b16 v[206:207], v213 offset:0x200
	ds_read_b64_tr_b16 v[208:209], v213 offset:0x1200
	ds_read_b64_tr_b16 v[238:239], v213 offset:0x2200
	ds_read_b64_tr_b16 v[240:241], v213 offset:0x3200
	ds_read_b64_tr_b16 v[244:245], v213 offset:0x4200
	ds_read_b64_tr_b16 v[246:247], v213 offset:0x5200
	ds_read_b64_tr_b16 v[250:251], v213 offset:0x6200
	ds_read_b64_tr_b16 v[252:253], v213 offset:0x7200
	s_waitcnt lgkmcnt(0)
	s_nop 0
	v_mfma_f32_32x32x16_bf16 v[98:113], v[130:133], v[206:209], v[98:113]
	ds_read_b64_tr_b16 v[206:207], v213 offset:0x400
	ds_read_b64_tr_b16 v[208:209], v213 offset:0x1400
	v_mfma_f32_32x32x16_bf16 v[98:113], v[134:137], v[238:241], v[98:113]
	ds_read_b64_tr_b16 v[238:239], v213 offset:0x2400
	ds_read_b64_tr_b16 v[240:241], v213 offset:0x3400
	v_mfma_f32_32x32x16_bf16 v[98:113], v[138:141], v[244:247], v[98:113]
	ds_read_b64_tr_b16 v[244:245], v213 offset:0x4400
	ds_read_b64_tr_b16 v[246:247], v213 offset:0x5400
	v_mfma_f32_32x32x16_bf16 v[98:113], v[142:145], v[250:253], v[98:113]
	ds_read_b64_tr_b16 v[250:251], v213 offset:0x6400
	ds_read_b64_tr_b16 v[252:253], v213 offset:0x7400
	s_waitcnt lgkmcnt(0)
	v_mfma_f32_32x32x16_bf16 v[82:97], v[130:133], v[206:209], v[82:97]
	ds_read_b64_tr_b16 v[206:207], v213 offset:0x600
	ds_read_b64_tr_b16 v[208:209], v213 offset:0x1600
	v_mfma_f32_32x32x16_bf16 v[82:97], v[134:137], v[238:241], v[82:97]
	ds_read_b64_tr_b16 v[238:239], v213 offset:0x2600
	ds_read_b64_tr_b16 v[240:241], v213 offset:0x3600
	v_mfma_f32_32x32x16_bf16 v[82:97], v[138:141], v[244:247], v[82:97]
	ds_read_b64_tr_b16 v[244:245], v213 offset:0x4600
	ds_read_b64_tr_b16 v[246:247], v213 offset:0x5600
	v_mfma_f32_32x32x16_bf16 v[82:97], v[142:145], v[250:253], v[82:97]
	ds_read_b64_tr_b16 v[250:251], v213 offset:0x6600
	ds_read_b64_tr_b16 v[252:253], v213 offset:0x7600
	s_waitcnt lgkmcnt(0)
	v_mfma_f32_32x32x16_bf16 v[66:81], v[130:133], v[206:209], v[66:81]
	ds_read_b64_tr_b16 v[206:207], v213 offset:0x800
	ds_read_b64_tr_b16 v[208:209], v213 offset:0x1800
	v_mfma_f32_32x32x16_bf16 v[66:81], v[134:137], v[238:241], v[66:81]
	ds_read_b64_tr_b16 v[238:239], v213 offset:0x2800
	ds_read_b64_tr_b16 v[240:241], v213 offset:0x3800
	v_mfma_f32_32x32x16_bf16 v[66:81], v[138:141], v[244:247], v[66:81]
	ds_read_b64_tr_b16 v[244:245], v213 offset:0x4800
	ds_read_b64_tr_b16 v[246:247], v213 offset:0x5800
	v_mfma_f32_32x32x16_bf16 v[66:81], v[142:145], v[250:253], v[66:81]
	ds_read_b64_tr_b16 v[250:251], v213 offset:0x6800
	ds_read_b64_tr_b16 v[252:253], v213 offset:0x7800
	s_waitcnt lgkmcnt(0)
	v_mfma_f32_32x32x16_bf16 v[50:65], v[130:133], v[206:209], v[50:65]
	ds_read_b64_tr_b16 v[206:207], v213 offset:0xa00
	ds_read_b64_tr_b16 v[208:209], v213 offset:0x1a00
	v_mfma_f32_32x32x16_bf16 v[50:65], v[134:137], v[238:241], v[50:65]
	ds_read_b64_tr_b16 v[238:239], v213 offset:0x2a00
	ds_read_b64_tr_b16 v[240:241], v213 offset:0x3a00
	v_mfma_f32_32x32x16_bf16 v[50:65], v[138:141], v[244:247], v[50:65]
	ds_read_b64_tr_b16 v[244:245], v213 offset:0x4a00
	ds_read_b64_tr_b16 v[246:247], v213 offset:0x5a00
	v_mfma_f32_32x32x16_bf16 v[50:65], v[142:145], v[250:253], v[50:65]
	ds_read_b64_tr_b16 v[250:251], v213 offset:0x6a00
	ds_read_b64_tr_b16 v[252:253], v213 offset:0x7a00
	s_waitcnt lgkmcnt(0)
	v_mfma_f32_32x32x16_bf16 v[34:49], v[130:133], v[206:209], v[34:49]
	ds_read_b64_tr_b16 v[206:207], v213 offset:0xc00
	ds_read_b64_tr_b16 v[208:209], v213 offset:0x1c00
	v_mfma_f32_32x32x16_bf16 v[34:49], v[134:137], v[238:241], v[34:49]
	ds_read_b64_tr_b16 v[238:239], v213 offset:0x2c00
	ds_read_b64_tr_b16 v[240:241], v213 offset:0x3c00
	v_mfma_f32_32x32x16_bf16 v[34:49], v[138:141], v[244:247], v[34:49]
	ds_read_b64_tr_b16 v[244:245], v213 offset:0x4c00
	ds_read_b64_tr_b16 v[246:247], v213 offset:0x5c00
	v_mfma_f32_32x32x16_bf16 v[34:49], v[142:145], v[250:253], v[34:49]
	ds_read_b64_tr_b16 v[250:251], v213 offset:0x6c00
	ds_read_b64_tr_b16 v[252:253], v213 offset:0x7c00
	s_waitcnt lgkmcnt(0)
	v_mfma_f32_32x32x16_bf16 v[18:33], v[130:133], v[206:209], v[18:33]
	ds_read_b64_tr_b16 v[206:207], v213 offset:0xe00
	ds_read_b64_tr_b16 v[208:209], v213 offset:0x1e00
	v_mfma_f32_32x32x16_bf16 v[18:33], v[134:137], v[238:241], v[18:33]
	ds_read_b64_tr_b16 v[238:239], v213 offset:0x2e00
	ds_read_b64_tr_b16 v[240:241], v213 offset:0x3e00
	v_mfma_f32_32x32x16_bf16 v[18:33], v[138:141], v[244:247], v[18:33]
	ds_read_b64_tr_b16 v[244:245], v213 offset:0x4e00
	ds_read_b64_tr_b16 v[246:247], v213 offset:0x5e00
	v_mfma_f32_32x32x16_bf16 v[18:33], v[142:145], v[250:253], v[18:33]
	ds_read_b64_tr_b16 v[250:251], v213 offset:0x6e00
	ds_read_b64_tr_b16 v[252:253], v213 offset:0x7e00
	s_waitcnt lgkmcnt(0)
	v_mfma_f32_32x32x16_bf16 v[2:17], v[130:133], v[206:209], v[2:17]
	v_mfma_f32_32x32x16_bf16 v[2:17], v[134:137], v[238:241], v[2:17]
	v_mfma_f32_32x32x16_bf16 v[2:17], v[138:141], v[244:247], v[2:17]
	v_mfma_f32_32x32x16_bf16 v[2:17], v[142:145], v[250:253], v[2:17]
	s_setprio 0
	v_add_u32_e32 v227, 0x14000, v225
	s_waitcnt vmcnt(0)
	s_waitcnt vmcnt(1)
	ds_write_b128 v227, v[182:185]
	s_waitcnt vmcnt(0)
	ds_write_b128 v227, v[186:189] offset:8192
	ds_write_b128 v220, v[146:149] offset:32768
	ds_write_b128 v220, v[158:161] offset:49152
	ds_write_b128 v220, v[150:153] offset:34816
	ds_write_b128 v220, v[154:157] offset:51200
	v_subrev_u32_e32 v182, 64, v226
	v_cvt_f32_i32_e32 v130, v182
	s_waitcnt lgkmcnt(0)
	s_barrier
	v_readlane_b32 s98, v255, 63
	s_bitcmp1_b32 s98, 0
	s_cbranch_scc0 .Ldsy_1
	s_sleep 6
.Ldsy_1:
	v_mul_f32_e64 v146, -v190, v130
	s_mov_b32 s2, 0x41900000
	s_mov_b32 s3, 0x41980000
	v_pk_fma_f32 v[140:141], v[196:197], s[2:3], v[146:147] op_sel_hi:[1,1,0]
	s_mov_b32 s2, 0x41c00000
	s_mov_b32 s3, 0x41c80000
	v_pk_fma_f32 v[142:143], v[196:197], s[2:3], v[146:147] op_sel_hi:[1,1,0]
	s_mov_b32 s2, 0x41d00000
	s_mov_b32 s3, 0x41d80000
	v_pk_fma_f32 v[144:145], v[196:197], s[2:3], v[146:147] op_sel_hi:[1,1,0]
	s_mov_b32 s2, 0x42000000
	v_fma_f32 v131, -v190, v130, v190
	v_mov_b32_e32 v130, v146
	v_mov_b32_e32 v191, v190
	s_mov_b32 s3, 0x42040000
	v_fmac_f32_e32 v130, 0, v190
	v_pk_fma_f32 v[132:133], v[196:197], s[60:61], v[146:147] op_sel_hi:[1,1,0]
	v_pk_fma_f32 v[134:135], v[196:197], s[74:75], v[146:147] op_sel_hi:[1,1,0]
	v_pk_fma_f32 v[136:137], v[196:197], s[62:63], v[146:147] op_sel_hi:[1,1,0]
	v_pk_fma_f32 v[138:139], v[196:197], s[58:59], v[146:147] op_sel_hi:[1,1,0]
	v_pk_fma_f32 v[160:161], v[190:191], s[68:69], v[146:147] op_sel_hi:[1,1,0]
	v_pk_fma_f32 v[158:159], v[190:191], s[96:97], v[146:147] op_sel_hi:[1,1,0]
	v_pk_fma_f32 v[156:157], v[190:191], s[94:95], v[146:147] op_sel_hi:[1,1,0]
	v_pk_fma_f32 v[154:155], v[190:191], s[92:93], v[146:147] op_sel_hi:[1,1,0]
	v_pk_fma_f32 v[152:153], v[190:191], s[90:91], v[146:147] op_sel_hi:[1,1,0]
	v_pk_fma_f32 v[150:151], v[190:191], s[88:89], v[146:147] op_sel_hi:[1,1,0]
	v_pk_fma_f32 v[148:149], v[190:191], s[86:87], v[146:147] op_sel_hi:[1,1,0]
	v_pk_fma_f32 v[146:147], v[192:193], s[2:3], v[146:147] op_sel_hi:[1,1,0]
	s_setprio 1
	ds_read_b128 v[206:209], v205
	ds_read_b128 v[250:253], v205 offset:1024
	ds_read_b128 v[184:187], v218
	ds_read_b128 v[238:241], v218 offset:8192
	ds_read_b128 v[244:247], v217
	s_waitcnt lgkmcnt(2)
	v_mfma_f32_32x32x16_bf16 v[130:145], v[184:187], v[178:181], v[130:145]
	ds_read_b128 v[184:187], v217 offset:8192
	s_waitcnt lgkmcnt(2)
	v_mfma_f32_32x32x16_bf16 v[146:161], v[238:241], v[178:181], v[146:161]
	ds_read_b128 v[238:241], v216
	s_waitcnt lgkmcnt(2)
	v_mfma_f32_32x32x16_bf16 v[130:145], v[244:247], v[170:173], v[130:145]
	ds_read_b128 v[244:247], v216 offset:8192
	s_waitcnt lgkmcnt(2)
	v_mfma_f32_32x32x16_bf16 v[146:161], v[184:187], v[170:173], v[146:161]
	ds_read_b128 v[184:187], v215
	s_waitcnt lgkmcnt(2)
	v_mfma_f32_32x32x16_bf16 v[130:145], v[238:241], v[166:169], v[130:145]
	ds_read_b128 v[238:241], v215 offset:8192
	s_waitcnt lgkmcnt(2)
	v_mfma_f32_32x32x16_bf16 v[146:161], v[244:247], v[166:169], v[146:161]
	ds_read_b128 v[244:247], v218 offset:128
	s_waitcnt lgkmcnt(2)
	v_mfma_f32_32x32x16_bf16 v[130:145], v[184:187], v[162:165], v[130:145]
	ds_read_b128 v[184:187], v218 offset:8320
	s_waitcnt lgkmcnt(2)
	v_mfma_f32_32x32x16_bf16 v[146:161], v[238:241], v[162:165], v[146:161]
	ds_read_b128 v[238:241], v217 offset:128
	s_waitcnt lgkmcnt(2)
	v_mfma_f32_32x32x16_bf16 v[130:145], v[244:247], v[174:177], v[130:145]
	ds_read_b128 v[244:247], v217 offset:8320
	s_waitcnt lgkmcnt(2)
	v_mfma_f32_32x32x16_bf16 v[146:161], v[184:187], v[174:177], v[146:161]
	ds_read_b128 v[184:187], v216 offset:128
	s_waitcnt lgkmcnt(2)
	v_mfma_f32_32x32x16_bf16 v[130:145], v[238:241], v[206:209], v[130:145]
	ds_read_b128 v[238:241], v216 offset:8320
	s_waitcnt lgkmcnt(2)
	v_mfma_f32_32x32x16_bf16 v[146:161], v[244:247], v[206:209], v[146:161]
	ds_read_b128 v[244:247], v215 offset:128
	ds_read_b128 v[206:209], v205 offset:2048
	s_waitcnt lgkmcnt(3)
	v_mfma_f32_32x32x16_bf16 v[130:145], v[184:187], v[250:253], v[130:145]
	ds_read_b128 v[184:187], v215 offset:8320
	s_waitcnt lgkmcnt(3)
	v_mfma_f32_32x32x16_bf16 v[146:161], v[238:241], v[250:253], v[146:161]
	s_waitcnt lgkmcnt(1)
	v_mfma_f32_32x32x16_bf16 v[130:145], v[244:247], v[206:209], v[130:145]
	s_waitcnt lgkmcnt(0)
	v_mfma_f32_32x32x16_bf16 v[146:161], v[184:187], v[206:209], v[146:161]
	s_setprio 0
	s_sub_i32 s2, s85, 33
	s_cmp_le_i32 s2, s65
	s_cbranch_scc1 .LBB0_1362
	v_cmp_gt_i32_e64 s[60:61], 26, v182
	v_cmp_gt_i32_e64 s[62:63], 27, v182
	v_cmp_gt_i32_e64 s[58:59], 25, v182
	s_and_b64 s[60:61], s[62:63], s[60:61]
	v_cmp_gt_i32_e64 s[56:57], 24, v182
	s_and_b64 s[58:59], s[60:61], s[58:59]
	v_cmp_gt_i32_e64 s[54:55], 19, v182
	s_and_b64 s[56:57], s[58:59], s[56:57]
	v_cmp_gt_i32_e64 s[52:53], 18, v182
	s_and_b64 s[54:55], s[56:57], s[54:55]
	v_cmp_gt_i32_e64 s[50:51], 17, v182
	s_and_b64 s[52:53], s[54:55], s[52:53]
	v_cmp_gt_i32_e64 s[48:49], 16, v182
	s_and_b64 s[50:51], s[52:53], s[50:51]
	v_cmp_gt_i32_e64 s[46:47], 11, v182
	s_and_b64 s[48:49], s[50:51], s[48:49]
	v_cmp_gt_i32_e64 s[44:45], 10, v182
	s_and_b64 s[46:47], s[48:49], s[46:47]
	v_cmp_gt_i32_e64 s[42:43], 9, v182
	s_and_b64 s[44:45], s[46:47], s[44:45]
	v_cmp_gt_i32_e64 s[40:41], 8, v182
	s_and_b64 s[42:43], s[44:45], s[42:43]
	v_cmp_gt_i32_e64 s[38:39], 3, v182
	s_and_b64 s[40:41], s[42:43], s[40:41]
	v_cmp_gt_i32_e64 s[36:37], 2, v182
	s_and_b64 s[38:39], s[40:41], s[38:39]
	v_cmp_gt_i32_e64 s[34:35], 1, v182
	s_and_b64 s[36:37], s[38:39], s[36:37]
	v_cmp_gt_i32_e64 s[30:31], 0, v182
	s_and_b64 s[34:35], s[36:37], s[34:35]
	s_and_b64 s[30:31], s[34:35], s[30:31]
	v_cmp_gt_i32_e64 s[28:29], 58, v182
	v_cndmask_b32_e64 v130, v130, v243, s[30:31]
	v_cmp_gt_i32_e64 s[30:31], 59, v182
	v_cmp_gt_i32_e64 s[26:27], 57, v182
	s_and_b64 s[28:29], s[30:31], s[28:29]
	v_cmp_gt_i32_e64 s[24:25], 56, v182
	s_and_b64 s[26:27], s[28:29], s[26:27]
	v_cmp_gt_i32_e64 s[22:23], 51, v182
	s_and_b64 s[24:25], s[26:27], s[24:25]
	v_cmp_gt_i32_e64 s[20:21], 50, v182
	s_and_b64 s[22:23], s[24:25], s[22:23]
	v_cmp_gt_i32_e64 s[18:19], 49, v182
	s_and_b64 s[20:21], s[22:23], s[20:21]
	v_cmp_gt_i32_e64 s[16:17], 48, v182
	s_and_b64 s[18:19], s[20:21], s[18:19]
	v_cmp_gt_i32_e64 s[14:15], 43, v182
	s_and_b64 s[16:17], s[18:19], s[16:17]
	v_cmp_gt_i32_e64 s[12:13], 42, v182
	s_and_b64 s[14:15], s[16:17], s[14:15]
	v_cmp_gt_i32_e64 s[10:11], 41, v182
	s_and_b64 s[12:13], s[14:15], s[12:13]
	v_cmp_gt_i32_e64 s[8:9], 40, v182
	s_and_b64 s[10:11], s[12:13], s[10:11]
	v_cmp_gt_i32_e64 s[6:7], 35, v182
	s_and_b64 s[8:9], s[10:11], s[8:9]
	v_cmp_gt_i32_e64 s[4:5], 34, v182
	s_and_b64 s[6:7], s[8:9], s[6:7]
	v_cmp_gt_i32_e64 s[2:3], 33, v182
	s_and_b64 s[4:5], s[6:7], s[4:5]
	v_cmp_gt_i32_e32 vcc, 32, v182
	s_and_b64 s[2:3], s[4:5], s[2:3]
	v_cndmask_b32_e64 v145, v145, v243, s[62:63]
	s_mov_b32 s62, 0x41200000
	v_cndmask_b32_e64 v144, v144, v243, s[60:61]
	s_mov_b32 s60, 2.0
	v_cndmask_b32_e64 v143, v143, v243, s[58:59]
	s_mov_b32 s58, 0x41800000
	s_and_b64 vcc, s[2:3], vcc
	s_mov_b32 s63, 0x41300000
	s_mov_b32 s61, 0x40400000
	s_mov_b32 s59, 0x41880000
	v_cndmask_b32_e64 v142, v142, v243, s[56:57]
	v_cndmask_b32_e64 v141, v141, v243, s[54:55]
	v_cndmask_b32_e64 v140, v140, v243, s[52:53]
	v_cndmask_b32_e64 v139, v139, v243, s[50:51]
	v_cndmask_b32_e64 v138, v138, v243, s[48:49]
	v_cndmask_b32_e64 v137, v137, v243, s[46:47]
	v_cndmask_b32_e64 v136, v136, v243, s[44:45]
	v_cndmask_b32_e64 v135, v135, v243, s[42:43]
	v_cndmask_b32_e64 v134, v134, v243, s[40:41]
	v_cndmask_b32_e64 v133, v133, v243, s[38:39]
	v_cndmask_b32_e64 v132, v132, v243, s[36:37]
	v_cndmask_b32_e64 v131, v131, v243, s[34:35]
	v_cndmask_b32_e64 v161, v161, v243, s[30:31]
	v_cndmask_b32_e64 v160, v160, v243, s[28:29]
	v_cndmask_b32_e64 v159, v159, v243, s[26:27]
	v_cndmask_b32_e64 v158, v158, v243, s[24:25]
	v_cndmask_b32_e64 v157, v157, v243, s[22:23]
	v_cndmask_b32_e64 v156, v156, v243, s[20:21]
	v_cndmask_b32_e64 v155, v155, v243, s[18:19]
	v_cndmask_b32_e64 v154, v154, v243, s[16:17]
	v_cndmask_b32_e64 v153, v153, v243, s[14:15]
	v_cndmask_b32_e64 v152, v152, v243, s[12:13]
	v_cndmask_b32_e64 v151, v151, v243, s[10:11]
	v_cndmask_b32_e64 v150, v150, v243, s[8:9]
	v_cndmask_b32_e64 v149, v149, v243, s[6:7]
	v_cndmask_b32_e64 v148, v148, v243, s[4:5]
	v_cndmask_b32_e64 v147, v147, v243, s[2:3]
	v_cndmask_b32_e32 v146, v146, v243, vcc
